# MoE epilogues: the full vmcnt drain that covers the next unit's bias preload sits mid-epilogue (after half of the stores) instead of at the unit top / before the first store
# speedup vs baseline: 1.0032x; 1.0032x over previous
; __device__ __forceinline__ u32x4 pack8(const f32x4 v0, const f32x4 v1) { u32x4 w; w.x = cvt_pk_bf16(v0[0], v0[1]); w.y = cvt_pk_bf16(v0[2], v0[3]); w.z = cvt_pk_bf16(v1[0], v1[1]); w.w = cvt_pk_bf16(v1[2], v1[3]); return w; }
;     __device__ __forceinline__ void operator()(const f32x4 (&acc)[2][2][4][2], const Unit& u, int wr, int wc, int fr, int fq) const {
;         const int row0 = u.pm * BM + wr * 64 + fr, f0 = u.pn * HALF + wc * 32 + 8 * fq;
; #pragma unroll
;         for (int ai = 0; ai < 2; ++ai)
; #pragma unroll
;             for (int m = 0; m < 4; ++m) {
;                 f32x4 o[2];
; #pragma unroll
;                 for (int n = 0; n < 2; ++n) { const f32x4 g4 = acc[ai][0][m][n], u4 = acc[ai][1][m][n];
; #pragma unroll
;                     for (int i = 0; i < 4; i += 2) {
;                         typedef float f32x2p __attribute__((ext_vector_type(2)));
;                         const f32x2p g = {__builtin_amdgcn_fmed3f(g4[i], -3.0e38f, 7.0f), __builtin_amdgcn_fmed3f(g4[i + 1], -3.0e38f, 7.0f)}, up = {__builtin_amdgcn_fmed3f(u4[i], -7.0f, 7.0f), __builtin_amdgcn_fmed3f(u4[i + 1], -7.0f, 7.0f)};
;                         const f32x2p a = g * (f32x2p){-1.702f * 1.4426950408889634f, -1.702f * 1.4426950408889634f};
;                         const f32x2p d = (f32x2p){__builtin_amdgcn_exp2f(a.x), __builtin_amdgcn_exp2f(a.y)} + (f32x2p){1.0f, 1.0f};
;                         const f32x2p t = g * (f32x2p){__builtin_amdgcn_rcpf(d.x), __builtin_amdgcn_rcpf(d.y)};
;                         const f32x2p r = __builtin_elementwise_fma(t, up, t); o[n][i] = r.x; o[n][i + 1] = r.y; } }
;                 *(u32x4*)(ACT + (size_t)(row0 + ai * HALF + m * 16) * 1024 + f0) = pack8(o[0], o[1]); }
.LBB0_1099:
	s_add_u32 s8, s21, 0xffffff00
	s_addc_u32 s9, s37, -1
	s_ashr_i32 s69, s68, 31
	s_lshl_b64 s[10:11], s[68:69], 13
	s_add_u32 s2, s75, s10
	s_addc_u32 s12, s50, s11
	s_lshl_b32 s10, s63, 7
	s_ashr_i32 s11, s10, 31
	s_lshl_b64 s[10:11], s[10:11], 2
	s_add_u32 s2, s2, s10
	s_addc_u32 s11, s12, s11
	s_add_u32 s10, s2, s42
	s_addc_u32 s11, s11, 0
	v_mov_b32_e32 v147, v1
	v_lshl_add_u64 v[138:139], s[10:11], 0, v[146:147]
	global_load_dwordx4 v[130:133], v146, s[10:11] offset:16
	global_load_dwordx4 v[134:137], v146, s[10:11]
	s_mov_b64 s[10:11], 0x1000
	s_movk_i32 s2, 0x1000
	v_lshl_add_u64 v[140:141], v[138:139], 0, s[10:11]
	v_add_co_u32_e32 v138, vcc, s2, v138
	s_nop 1
	v_addc_co_u32_e32 v139, vcc, 0, v139, vcc
	global_load_dwordx4 v[142:145], v[138:139], off
	s_nop 0
	global_load_dwordx4 v[138:141], v[140:141], off offset:16
	v_med3_f32 v166, v122, s57, v234
	v_med3_f32 v167, v123, s57, v234
	v_pk_mul_f32 v[182:183], v[166:167], s[96:97] op_sel_hi:[1,0]
	v_med3_f32 v180, v78, s33, v234
	v_exp_f32_e32 v182, v182
	v_exp_f32_e32 v183, v183
	v_med3_f32 v181, v79, s33, v234
	v_lshl_add_u32 v164, s62, 8, v153
	v_lshl_or_b32 v162, s90, 7, v179
	v_pk_add_f32 v[182:183], v[182:183], 1.0 op_sel_hi:[1,0]
	v_ashrrev_i32_e32 v165, 31, v164
	v_rcp_f32_e32 v182, v182
	v_rcp_f32_e32 v183, v183
	v_ashrrev_i32_e32 v163, 31, v162
	s_mov_b32 s2, 0x40000
	v_pk_mul_f32 v[166:167], v[166:167], v[182:183]
	s_nop 0
	v_pk_fma_f32 v[166:167], v[166:167], v[180:181], v[166:167]
	v_med3_f32 v180, v124, s57, v234
	v_med3_f32 v181, v125, s57, v234
	v_pk_mul_f32 v[188:189], v[180:181], s[96:97] op_sel_hi:[1,0]
	v_med3_f32 v182, v80, s33, v234
	v_exp_f32_e32 v188, v188
	v_exp_f32_e32 v189, v189
	v_med3_f32 v183, v81, s33, v234
	v_pk_add_f32 v[188:189], v[188:189], 1.0 op_sel_hi:[1,0]
	s_nop 0
	v_rcp_f32_e32 v188, v188
	v_rcp_f32_e32 v189, v189
	s_nop 0
	v_pk_mul_f32 v[180:181], v[180:181], v[188:189]
	s_nop 0
	v_pk_fma_f32 v[182:183], v[180:181], v[182:183], v[180:181]
	v_med3_f32 v180, v114, s57, v234
	v_med3_f32 v181, v115, s57, v234
	v_pk_mul_f32 v[190:191], v[180:181], s[96:97] op_sel_hi:[1,0]
	v_med3_f32 v188, v74, s33, v234
	v_exp_f32_e32 v190, v190
	v_exp_f32_e32 v191, v191
	v_med3_f32 v189, v75, s33, v234
	v_pk_add_f32 v[190:191], v[190:191], 1.0 op_sel_hi:[1,0]
	s_nop 0
	v_rcp_f32_e32 v190, v190
	v_rcp_f32_e32 v191, v191
	s_nop 0
	v_pk_mul_f32 v[180:181], v[180:181], v[190:191]
	s_nop 0
	v_pk_fma_f32 v[188:189], v[180:181], v[188:189], v[180:181]
	v_med3_f32 v180, v116, s57, v234
	v_med3_f32 v181, v117, s57, v234
	v_pk_mul_f32 v[192:193], v[180:181], s[96:97] op_sel_hi:[1,0]
	v_med3_f32 v190, v76, s33, v234
	v_exp_f32_e32 v192, v192
	v_exp_f32_e32 v193, v193
	v_med3_f32 v191, v77, s33, v234
	v_pk_add_f32 v[192:193], v[192:193], 1.0 op_sel_hi:[1,0]
	s_nop 0
	v_rcp_f32_e32 v192, v192
	v_rcp_f32_e32 v193, v193
	s_nop 0
	v_pk_mul_f32 v[180:181], v[180:181], v[192:193]
	s_nop 0
	v_pk_fma_f32 v[190:191], v[180:181], v[190:191], v[180:181]
	v_cvt_pk_bf16_f32 v180, v166, v167
	v_lshlrev_b64 v[166:167], 11, v[164:165]
	v_cvt_pk_bf16_f32 v181, v182, v183
	v_cvt_pk_bf16_f32 v182, v188, v189
	v_lshl_add_u64 v[188:189], s[28:29], 0, v[166:167]
	v_lshlrev_b64 v[166:167], 1, v[162:163]
	v_lshl_add_u64 v[162:163], v[188:189], 0, v[166:167]
	v_cvt_pk_bf16_f32 v183, v190, v191
	global_store_dwordx4 v[162:163], v[180:183], off
	s_nop 1
	v_med3_f32 v180, v106, s57, v234
	v_med3_f32 v181, v107, s57, v234
	v_pk_mul_f32 v[188:189], v[180:181], s[96:97] op_sel_hi:[1,0]
	v_med3_f32 v182, v70, s33, v234
	v_exp_f32_e32 v188, v188
	v_exp_f32_e32 v189, v189
	v_med3_f32 v183, v71, s33, v234
	v_pk_add_f32 v[188:189], v[188:189], 1.0 op_sel_hi:[1,0]
	s_nop 0
	v_rcp_f32_e32 v188, v188
	v_rcp_f32_e32 v189, v189
	s_nop 0
	v_pk_mul_f32 v[180:181], v[180:181], v[188:189]
	s_nop 0
	v_pk_fma_f32 v[180:181], v[180:181], v[182:183], v[180:181]
	v_med3_f32 v182, v108, s57, v234
	v_med3_f32 v183, v109, s57, v234
	v_pk_mul_f32 v[190:191], v[182:183], s[96:97] op_sel_hi:[1,0]
	v_med3_f32 v188, v72, s33, v234
	v_exp_f32_e32 v190, v190
	v_exp_f32_e32 v191, v191
	v_med3_f32 v189, v73, s33, v234
	v_cvt_pk_bf16_f32 v180, v180, v181
	v_pk_add_f32 v[190:191], v[190:191], 1.0 op_sel_hi:[1,0]
	s_nop 0
	v_rcp_f32_e32 v190, v190
	v_rcp_f32_e32 v191, v191
	s_nop 0
	v_pk_mul_f32 v[182:183], v[182:183], v[190:191]
	s_nop 0
	v_pk_fma_f32 v[182:183], v[182:183], v[188:189], v[182:183]
	v_med3_f32 v188, v98, s57, v234
	v_med3_f32 v189, v99, s57, v234
	v_pk_mul_f32 v[192:193], v[188:189], s[96:97] op_sel_hi:[1,0]
	v_med3_f32 v190, v66, s33, v234
	v_exp_f32_e32 v192, v192
	v_exp_f32_e32 v193, v193
	v_med3_f32 v191, v67, s33, v234
	v_cvt_pk_bf16_f32 v181, v182, v183
	v_pk_add_f32 v[192:193], v[192:193], 1.0 op_sel_hi:[1,0]
	s_nop 0
	v_rcp_f32_e32 v192, v192
	v_rcp_f32_e32 v193, v193
	s_nop 0
	v_pk_mul_f32 v[188:189], v[188:189], v[192:193]
	s_nop 0
	v_pk_fma_f32 v[188:189], v[188:189], v[190:191], v[188:189]
	v_med3_f32 v190, v100, s57, v234
	v_med3_f32 v191, v101, s57, v234
	v_pk_mul_f32 v[194:195], v[190:191], s[96:97] op_sel_hi:[1,0]
	v_cvt_pk_bf16_f32 v182, v188, v189
	v_or_b32_e32 v188, 16, v164
	v_exp_f32_e32 v194, v194
	v_exp_f32_e32 v195, v195
	v_ashrrev_i32_e32 v189, 31, v188
	v_lshlrev_b64 v[188:189], 11, v[188:189]
	v_lshl_add_u64 v[188:189], s[28:29], 0, v[188:189]
	v_pk_add_f32 v[194:195], v[194:195], 1.0 op_sel_hi:[1,0]
	v_med3_f32 v192, v68, s33, v234
	v_rcp_f32_e32 v194, v194
	v_rcp_f32_e32 v195, v195
	v_med3_f32 v193, v69, s33, v234
	v_lshl_add_u64 v[188:189], v[188:189], 0, v[166:167]
	v_pk_mul_f32 v[190:191], v[190:191], v[194:195]
	s_nop 0
	v_pk_fma_f32 v[190:191], v[190:191], v[192:193], v[190:191]
; __device__ __forceinline__ u32x4 pack8(const f32x4 v0, const f32x4 v1) { u32x4 w; w.x = cvt_pk_bf16(v0[0], v0[1]); w.y = cvt_pk_bf16(v0[2], v0[3]); w.z = cvt_pk_bf16(v1[0], v1[1]); w.w = cvt_pk_bf16(v1[2], v1[3]); return w; }
;     __device__ __forceinline__ void operator()(const f32x4 (&acc)[2][2][4][2], const Unit& u, int wr, int wc, int fr, int fq) const {
;     ...
;             for (int m = 0; m < 4; ++m) {
;                 f32x4 o[2];
; #pragma unroll
;                 for (int n = 0; n < 2; ++n) { const f32x4 g4 = acc[ai][0][m][n], u4 = acc[ai][1][m][n];
; #pragma unroll
;                     for (int i = 0; i < 4; i += 2) {
;                         typedef float f32x2p __attribute__((ext_vector_type(2)));
;                         const f32x2p g = {__builtin_amdgcn_fmed3f(g4[i], -3.0e38f, 7.0f), __builtin_amdgcn_fmed3f(g4[i + 1], -3.0e38f, 7.0f)}, up = {__builtin_amdgcn_fmed3f(u4[i], -7.0f, 7.0f), __builtin_amdgcn_fmed3f(u4[i + 1], -7.0f, 7.0f)};
;                         const f32x2p a = g * (f32x2p){-1.702f * 1.4426950408889634f, -1.702f * 1.4426950408889634f};
;                         const f32x2p d = (f32x2p){__builtin_amdgcn_exp2f(a.x), __builtin_amdgcn_exp2f(a.y)} + (f32x2p){1.0f, 1.0f};
;                         const f32x2p t = g * (f32x2p){__builtin_amdgcn_rcpf(d.x), __builtin_amdgcn_rcpf(d.y)};
;                         const f32x2p r = __builtin_elementwise_fma(t, up, t); o[n][i] = r.x; o[n][i + 1] = r.y; } }
;                 *(u32x4*)(ACT + (size_t)(row0 + ai * HALF + m * 16) * 1024 + f0) = pack8(o[0], o[1]); }
	s_nop 0
	v_cvt_pk_bf16_f32 v183, v190, v191
	global_store_dwordx4 v[188:189], v[180:183], off
	s_nop 1
	v_med3_f32 v180, v94, s57, v234
	v_med3_f32 v181, v95, s57, v234
	v_pk_mul_f32 v[188:189], v[180:181], s[96:97] op_sel_hi:[1,0]
	v_med3_f32 v182, v62, s33, v234
	v_exp_f32_e32 v188, v188
	v_exp_f32_e32 v189, v189
	v_med3_f32 v183, v63, s33, v234
	v_pk_add_f32 v[188:189], v[188:189], 1.0 op_sel_hi:[1,0]
	s_nop 0
	v_rcp_f32_e32 v188, v188
	v_rcp_f32_e32 v189, v189
	s_nop 0
	v_pk_mul_f32 v[180:181], v[180:181], v[188:189]
	s_nop 0
	v_pk_fma_f32 v[180:181], v[180:181], v[182:183], v[180:181]
	v_med3_f32 v182, v96, s57, v234
	v_med3_f32 v183, v97, s57, v234
	v_pk_mul_f32 v[190:191], v[182:183], s[96:97] op_sel_hi:[1,0]
	v_med3_f32 v188, v64, s33, v234
	v_exp_f32_e32 v190, v190
	v_exp_f32_e32 v191, v191
	v_med3_f32 v189, v65, s33, v234
	v_cvt_pk_bf16_f32 v180, v180, v181
	v_pk_add_f32 v[190:191], v[190:191], 1.0 op_sel_hi:[1,0]
	s_nop 0
	v_rcp_f32_e32 v190, v190
	v_rcp_f32_e32 v191, v191
	s_nop 0
	v_pk_mul_f32 v[182:183], v[182:183], v[190:191]
	s_nop 0
	v_pk_fma_f32 v[182:183], v[182:183], v[188:189], v[182:183]
	v_med3_f32 v188, v90, s57, v234
	v_med3_f32 v189, v91, s57, v234
	v_pk_mul_f32 v[192:193], v[188:189], s[96:97] op_sel_hi:[1,0]
	v_med3_f32 v190, v58, s33, v234
	v_exp_f32_e32 v192, v192
	v_exp_f32_e32 v193, v193
	v_med3_f32 v191, v59, s33, v234
	v_cvt_pk_bf16_f32 v181, v182, v183
	v_pk_add_f32 v[192:193], v[192:193], 1.0 op_sel_hi:[1,0]
	s_nop 0
	v_rcp_f32_e32 v192, v192
	v_rcp_f32_e32 v193, v193
	s_nop 0
	v_pk_mul_f32 v[188:189], v[188:189], v[192:193]
	s_nop 0
	v_pk_fma_f32 v[188:189], v[188:189], v[190:191], v[188:189]
	v_med3_f32 v190, v92, s57, v234
	v_med3_f32 v191, v93, s57, v234
	v_pk_mul_f32 v[194:195], v[190:191], s[96:97] op_sel_hi:[1,0]
	v_cvt_pk_bf16_f32 v182, v188, v189
	v_or_b32_e32 v188, 32, v164
	v_exp_f32_e32 v194, v194
	v_exp_f32_e32 v195, v195
	v_ashrrev_i32_e32 v189, 31, v188
	v_lshlrev_b64 v[188:189], 11, v[188:189]
	v_lshl_add_u64 v[188:189], s[28:29], 0, v[188:189]
	v_pk_add_f32 v[194:195], v[194:195], 1.0 op_sel_hi:[1,0]
	v_med3_f32 v192, v60, s33, v234
	v_rcp_f32_e32 v194, v194
	v_rcp_f32_e32 v195, v195
	v_med3_f32 v193, v61, s33, v234
	v_lshl_add_u64 v[188:189], v[188:189], 0, v[166:167]
	v_or_b32_e32 v164, 48, v164
	v_pk_mul_f32 v[190:191], v[190:191], v[194:195]
	v_ashrrev_i32_e32 v165, 31, v164
	v_pk_fma_f32 v[190:191], v[190:191], v[192:193], v[190:191]
	v_lshlrev_b64 v[164:165], 11, v[164:165]
	v_cvt_pk_bf16_f32 v183, v190, v191
	global_store_dwordx4 v[188:189], v[180:183], off
	v_lshl_add_u64 v[164:165], s[28:29], 0, v[164:165]
	v_lshl_add_u64 v[164:165], v[164:165], 0, v[166:167]
	v_med3_f32 v180, v86, s57, v234
	v_med3_f32 v181, v87, s57, v234
	v_pk_mul_f32 v[188:189], v[180:181], s[96:97] op_sel_hi:[1,0]
	v_med3_f32 v182, v54, s33, v234
	v_exp_f32_e32 v188, v188
	v_exp_f32_e32 v189, v189
	v_med3_f32 v183, v55, s33, v234
	v_med3_f32 v166, v22, s33, v234
	v_med3_f32 v167, v23, s33, v234
	v_pk_add_f32 v[188:189], v[188:189], 1.0 op_sel_hi:[1,0]
	s_nop 0
	v_rcp_f32_e32 v188, v188
	v_rcp_f32_e32 v189, v189
	s_nop 0
	v_pk_mul_f32 v[180:181], v[180:181], v[188:189]
	s_nop 0
	v_pk_fma_f32 v[180:181], v[180:181], v[182:183], v[180:181]
	v_med3_f32 v182, v88, s57, v234
	v_med3_f32 v183, v89, s57, v234
	v_pk_mul_f32 v[190:191], v[182:183], s[96:97] op_sel_hi:[1,0]
	v_med3_f32 v188, v56, s33, v234
	v_exp_f32_e32 v190, v190
	v_exp_f32_e32 v191, v191
	v_med3_f32 v189, v57, s33, v234
	v_cvt_pk_bf16_f32 v180, v180, v181
	v_pk_add_f32 v[190:191], v[190:191], 1.0 op_sel_hi:[1,0]
	s_nop 0
	v_rcp_f32_e32 v190, v190
	v_rcp_f32_e32 v191, v191
	s_nop 0
	v_pk_mul_f32 v[182:183], v[182:183], v[190:191]
	s_nop 0
	v_pk_fma_f32 v[182:183], v[182:183], v[188:189], v[182:183]
	v_med3_f32 v188, v82, s57, v234
	v_med3_f32 v189, v83, s57, v234
	v_pk_mul_f32 v[192:193], v[188:189], s[96:97] op_sel_hi:[1,0]
	v_med3_f32 v190, v50, s33, v234
	v_exp_f32_e32 v192, v192
	v_exp_f32_e32 v193, v193
	v_med3_f32 v191, v51, s33, v234
	v_cvt_pk_bf16_f32 v181, v182, v183
	v_pk_add_f32 v[192:193], v[192:193], 1.0 op_sel_hi:[1,0]
	s_nop 0
	v_rcp_f32_e32 v192, v192
	v_rcp_f32_e32 v193, v193
	s_nop 0
	v_pk_mul_f32 v[188:189], v[188:189], v[192:193]
	s_nop 0
	v_pk_fma_f32 v[188:189], v[188:189], v[190:191], v[188:189]
	v_med3_f32 v190, v84, s57, v234
	v_med3_f32 v191, v85, s57, v234
	v_pk_mul_f32 v[194:195], v[190:191], s[96:97] op_sel_hi:[1,0]
	v_med3_f32 v192, v52, s33, v234
	v_exp_f32_e32 v194, v194
	v_exp_f32_e32 v195, v195
	v_med3_f32 v193, v53, s33, v234
	v_cvt_pk_bf16_f32 v182, v188, v189
	v_pk_add_f32 v[194:195], v[194:195], 1.0 op_sel_hi:[1,0]
	s_nop 0
	v_rcp_f32_e32 v194, v194
	v_rcp_f32_e32 v195, v195
	s_nop 0
	v_pk_mul_f32 v[190:191], v[190:191], v[194:195]
	s_nop 0
	v_pk_fma_f32 v[190:191], v[190:191], v[192:193], v[190:191]
	s_nop 0
	v_cvt_pk_bf16_f32 v183, v190, v191
	global_store_dwordx4 v[164:165], v[180:183], off
	v_med3_f32 v164, v46, s57, v234
	v_med3_f32 v165, v47, s57, v234
	v_pk_mul_f32 v[180:181], v[164:165], s[96:97] op_sel_hi:[1,0]
	s_nop 0
	v_exp_f32_e32 v180, v180
	v_exp_f32_e32 v181, v181
	s_nop 0
	v_pk_add_f32 v[180:181], v[180:181], 1.0 op_sel_hi:[1,0]
	s_nop 0
	v_rcp_f32_e32 v180, v180
	v_rcp_f32_e32 v181, v181
	s_nop 0
	v_pk_mul_f32 v[164:165], v[164:165], v[180:181]
	s_nop 0
	v_pk_fma_f32 v[164:165], v[164:165], v[166:167], v[164:165]
	v_med3_f32 v166, v48, s57, v234
	v_med3_f32 v167, v49, s57, v234
	v_pk_mul_f32 v[182:183], v[166:167], s[96:97] op_sel_hi:[1,0]
	v_med3_f32 v180, v24, s33, v234
	v_exp_f32_e32 v182, v182
	v_exp_f32_e32 v183, v183
	v_med3_f32 v181, v25, s33, v234
	v_cvt_pk_bf16_f32 v164, v164, v165
; __device__ __forceinline__ u32x4 pack8(const f32x4 v0, const f32x4 v1) { u32x4 w; w.x = cvt_pk_bf16(v0[0], v0[1]); w.y = cvt_pk_bf16(v0[2], v0[3]); w.z = cvt_pk_bf16(v1[0], v1[1]); w.w = cvt_pk_bf16(v1[2], v1[3]); return w; }
;     __device__ __forceinline__ void operator()(const f32x4 (&acc)[2][2][4][2], const Unit& u, int wr, int wc, int fr, int fq) const {
;     ...
;             for (int m = 0; m < 4; ++m) {
;                 f32x4 o[2];
; #pragma unroll
;                 for (int n = 0; n < 2; ++n) { const f32x4 g4 = acc[ai][0][m][n], u4 = acc[ai][1][m][n];
; #pragma unroll
;                     for (int i = 0; i < 4; i += 2) {
;                         typedef float f32x2p __attribute__((ext_vector_type(2)));
;                         const f32x2p g = {__builtin_amdgcn_fmed3f(g4[i], -3.0e38f, 7.0f), __builtin_amdgcn_fmed3f(g4[i + 1], -3.0e38f, 7.0f)}, up = {__builtin_amdgcn_fmed3f(u4[i], -7.0f, 7.0f), __builtin_amdgcn_fmed3f(u4[i + 1], -7.0f, 7.0f)};
;                         const f32x2p a = g * (f32x2p){-1.702f * 1.4426950408889634f, -1.702f * 1.4426950408889634f};
;                         const f32x2p d = (f32x2p){__builtin_amdgcn_exp2f(a.x), __builtin_amdgcn_exp2f(a.y)} + (f32x2p){1.0f, 1.0f};
;                         const f32x2p t = g * (f32x2p){__builtin_amdgcn_rcpf(d.x), __builtin_amdgcn_rcpf(d.y)};
;                         const f32x2p r = __builtin_elementwise_fma(t, up, t); o[n][i] = r.x; o[n][i + 1] = r.y; } }
;                 *(u32x4*)(ACT + (size_t)(row0 + ai * HALF + m * 16) * 1024 + f0) = pack8(o[0], o[1]); }
	v_pk_add_f32 v[182:183], v[182:183], 1.0 op_sel_hi:[1,0]
	s_nop 0
	v_rcp_f32_e32 v182, v182
	v_rcp_f32_e32 v183, v183
	s_nop 0
	v_pk_mul_f32 v[166:167], v[166:167], v[182:183]
	s_nop 0
	v_pk_fma_f32 v[166:167], v[166:167], v[180:181], v[166:167]
	v_med3_f32 v180, v42, s57, v234
	v_med3_f32 v181, v43, s57, v234
	v_pk_mul_f32 v[188:189], v[180:181], s[96:97] op_sel_hi:[1,0]
	v_med3_f32 v182, v18, s33, v234
	v_exp_f32_e32 v188, v188
	v_exp_f32_e32 v189, v189
	v_med3_f32 v183, v19, s33, v234
	v_cvt_pk_bf16_f32 v165, v166, v167
	v_pk_add_f32 v[188:189], v[188:189], 1.0 op_sel_hi:[1,0]
	s_nop 0
	v_rcp_f32_e32 v188, v188
	v_rcp_f32_e32 v189, v189
	s_nop 0
	v_pk_mul_f32 v[180:181], v[180:181], v[188:189]
	s_nop 0
	v_pk_fma_f32 v[180:181], v[180:181], v[182:183], v[180:181]
	v_med3_f32 v182, v44, s57, v234
	v_med3_f32 v183, v45, s57, v234
	v_pk_mul_f32 v[190:191], v[182:183], s[96:97] op_sel_hi:[1,0]
	v_cvt_pk_bf16_f32 v166, v180, v181
	v_add_co_u32_e32 v180, vcc, s2, v162
	v_exp_f32_e32 v190, v190
	v_exp_f32_e32 v191, v191
	v_med3_f32 v188, v20, s33, v234
	v_med3_f32 v189, v21, s33, v234
	v_addc_co_u32_e32 v181, vcc, 0, v163, vcc
	v_pk_add_f32 v[190:191], v[190:191], 1.0 op_sel_hi:[1,0]
	s_mov_b32 s2, 0x48000
	v_rcp_f32_e32 v190, v190
	v_rcp_f32_e32 v191, v191
	s_nop 0
	v_pk_mul_f32 v[182:183], v[182:183], v[190:191]
	s_nop 0
	v_pk_fma_f32 v[182:183], v[182:183], v[188:189], v[182:183]
	s_nop 0
	v_cvt_pk_bf16_f32 v167, v182, v183
	s_waitcnt vmcnt(0)
; __device__ __forceinline__ u32x4 pack8(const f32x4 v0, const f32x4 v1) { u32x4 w; w.x = cvt_pk_bf16(v0[0], v0[1]); w.y = cvt_pk_bf16(v0[2], v0[3]); w.z = cvt_pk_bf16(v1[0], v1[1]); w.w = cvt_pk_bf16(v1[2], v1[3]); return w; }
; #define PG8_BAR __builtin_amdgcn_s_barrier()
;     __device__ __forceinline__ void operator()(const f32x4 (&acc)[2][2][4][2], const Unit& u, int wr, int wc, int fr, int fq) const {
;     ...
;             for (int m = 0; m < 4; ++m) {
;                 f32x4 o[2];
; #pragma unroll
;                 for (int n = 0; n < 2; ++n) { const f32x4 g4 = acc[ai][0][m][n], u4 = acc[ai][1][m][n];
; #pragma unroll
;                     for (int i = 0; i < 4; i += 2) {
;                         typedef float f32x2p __attribute__((ext_vector_type(2)));
;                         const f32x2p g = {__builtin_amdgcn_fmed3f(g4[i], -3.0e38f, 7.0f), __builtin_amdgcn_fmed3f(g4[i + 1], -3.0e38f, 7.0f)}, up = {__builtin_amdgcn_fmed3f(u4[i], -7.0f, 7.0f), __builtin_amdgcn_fmed3f(u4[i + 1], -7.0f, 7.0f)};
;                         const f32x2p a = g * (f32x2p){-1.702f * 1.4426950408889634f, -1.702f * 1.4426950408889634f};
;                         const f32x2p d = (f32x2p){__builtin_amdgcn_exp2f(a.x), __builtin_amdgcn_exp2f(a.y)} + (f32x2p){1.0f, 1.0f};
;                         const f32x2p t = g * (f32x2p){__builtin_amdgcn_rcpf(d.x), __builtin_amdgcn_rcpf(d.y)};
;                         const f32x2p r = __builtin_elementwise_fma(t, up, t); o[n][i] = r.x; o[n][i + 1] = r.y; } }
;                 *(u32x4*)(ACT + (size_t)(row0 + ai * HALF + m * 16) * 1024 + f0) = pack8(o[0], o[1]); }
; template <class Epi, class Sched, bool ALIGN_EPI = false, bool SP2 = false, bool GATHER = false>
; __device__ __forceinline__ void gemm_phase(PG8_LAS unsigned char* lds, const Gemm g, const Sched& S, const Epi& E, const int2* gslot = nullptr, PG8_LAS unsigned char* gtab = nullptr) {
;     ...
;         if constexpr (!Epi::AFTER_DRAIN) { E(acc, cur, wr, wc, fr, fq); S.done(cur); }
;         if (!has_next) break;
;         E.init(acc, pre);
;         cur = nxt; cA = nA; cB = nB; ++ui;
;         if constexpr (GATHER) { _Pragma("unroll") for (int h_ = 0; h_ < 2; ++h_) _Pragma("unroll") for (int i_ = 0; i_ < 2; ++i_) vC[h_][i_] = vN[h_][i_]; }
;         if constexpr (ALIGN_EPI) { if (wr == 1) PG8_BAR; }
	global_store_dwordx4 v[180:181], v[164:167], off
	s_nop 1
	v_med3_f32 v164, v38, s57, v234
	v_med3_f32 v165, v39, s57, v234
	v_pk_mul_f32 v[180:181], v[164:165], s[96:97] op_sel_hi:[1,0]
	v_med3_f32 v166, v14, s33, v234
	v_exp_f32_e32 v180, v180
	v_exp_f32_e32 v181, v181
	v_med3_f32 v167, v15, s33, v234
	v_pk_add_f32 v[180:181], v[180:181], 1.0 op_sel_hi:[1,0]
	s_nop 0
	v_rcp_f32_e32 v180, v180
	v_rcp_f32_e32 v181, v181
	s_nop 0
	v_pk_mul_f32 v[164:165], v[164:165], v[180:181]
	s_nop 0
	v_pk_fma_f32 v[164:165], v[164:165], v[166:167], v[164:165]
	v_med3_f32 v166, v40, s57, v234
	v_med3_f32 v167, v41, s57, v234
	v_pk_mul_f32 v[182:183], v[166:167], s[96:97] op_sel_hi:[1,0]
	v_med3_f32 v180, v16, s33, v234
	v_exp_f32_e32 v182, v182
	v_exp_f32_e32 v183, v183
	v_med3_f32 v181, v17, s33, v234
	v_cvt_pk_bf16_f32 v164, v164, v165
	v_pk_add_f32 v[182:183], v[182:183], 1.0 op_sel_hi:[1,0]
	s_nop 0
	v_rcp_f32_e32 v182, v182
	v_rcp_f32_e32 v183, v183
	s_nop 0
	v_pk_mul_f32 v[166:167], v[166:167], v[182:183]
	s_nop 0
	v_pk_fma_f32 v[166:167], v[166:167], v[180:181], v[166:167]
	v_med3_f32 v180, v34, s57, v234
	v_med3_f32 v181, v35, s57, v234
	v_pk_mul_f32 v[188:189], v[180:181], s[96:97] op_sel_hi:[1,0]
	v_med3_f32 v182, v10, s33, v234
	v_exp_f32_e32 v188, v188
	v_exp_f32_e32 v189, v189
	v_med3_f32 v183, v11, s33, v234
	v_cvt_pk_bf16_f32 v165, v166, v167
	v_pk_add_f32 v[188:189], v[188:189], 1.0 op_sel_hi:[1,0]
	s_nop 0
	v_rcp_f32_e32 v188, v188
	v_rcp_f32_e32 v189, v189
	s_nop 0
	v_pk_mul_f32 v[180:181], v[180:181], v[188:189]
	s_nop 0
	v_pk_fma_f32 v[180:181], v[180:181], v[182:183], v[180:181]
	v_med3_f32 v182, v36, s57, v234
	v_med3_f32 v183, v37, s57, v234
	v_pk_mul_f32 v[190:191], v[182:183], s[96:97] op_sel_hi:[1,0]
	v_cvt_pk_bf16_f32 v166, v180, v181
	v_add_co_u32_e32 v180, vcc, s2, v162
	v_exp_f32_e32 v190, v190
	v_exp_f32_e32 v191, v191
	v_med3_f32 v188, v12, s33, v234
	v_med3_f32 v189, v13, s33, v234
	v_addc_co_u32_e32 v181, vcc, 0, v163, vcc
	v_pk_add_f32 v[190:191], v[190:191], 1.0 op_sel_hi:[1,0]
	s_mov_b32 s2, 0x50000
	v_rcp_f32_e32 v190, v190
	v_rcp_f32_e32 v191, v191
	s_nop 0
	v_pk_mul_f32 v[182:183], v[182:183], v[190:191]
	s_nop 0
	v_pk_fma_f32 v[182:183], v[182:183], v[188:189], v[182:183]
	s_nop 0
	v_cvt_pk_bf16_f32 v167, v182, v183
	global_store_dwordx4 v[180:181], v[164:167], off
	s_nop 1
	v_med3_f32 v164, v30, s57, v234
	v_med3_f32 v165, v31, s57, v234
	v_pk_mul_f32 v[180:181], v[164:165], s[96:97] op_sel_hi:[1,0]
	v_med3_f32 v166, v102, s33, v234
	v_exp_f32_e32 v180, v180
	v_exp_f32_e32 v181, v181
	v_med3_f32 v167, v103, s33, v234
	v_pk_add_f32 v[180:181], v[180:181], 1.0 op_sel_hi:[1,0]
	s_nop 0
	v_rcp_f32_e32 v180, v180
	v_rcp_f32_e32 v181, v181
	s_nop 0
	v_pk_mul_f32 v[164:165], v[164:165], v[180:181]
	s_nop 0
	v_pk_fma_f32 v[164:165], v[164:165], v[166:167], v[164:165]
	v_med3_f32 v166, v32, s57, v234
	v_med3_f32 v167, v33, s57, v234
	v_pk_mul_f32 v[182:183], v[166:167], s[96:97] op_sel_hi:[1,0]
	v_med3_f32 v180, v104, s33, v234
	v_exp_f32_e32 v182, v182
	v_exp_f32_e32 v183, v183
	v_med3_f32 v181, v105, s33, v234
	v_cvt_pk_bf16_f32 v164, v164, v165
	v_pk_add_f32 v[182:183], v[182:183], 1.0 op_sel_hi:[1,0]
	s_nop 0
	v_rcp_f32_e32 v182, v182
	v_rcp_f32_e32 v183, v183
	s_nop 0
	v_pk_mul_f32 v[166:167], v[166:167], v[182:183]
	s_nop 0
	v_pk_fma_f32 v[166:167], v[166:167], v[180:181], v[166:167]
	v_med3_f32 v180, v26, s57, v234
	v_med3_f32 v181, v27, s57, v234
	v_pk_mul_f32 v[188:189], v[180:181], s[96:97] op_sel_hi:[1,0]
	v_med3_f32 v182, v110, s33, v234
	v_exp_f32_e32 v188, v188
	v_exp_f32_e32 v189, v189
	v_med3_f32 v183, v111, s33, v234
	v_cvt_pk_bf16_f32 v165, v166, v167
	v_pk_add_f32 v[188:189], v[188:189], 1.0 op_sel_hi:[1,0]
	s_nop 0
	v_rcp_f32_e32 v188, v188
	v_rcp_f32_e32 v189, v189
	s_nop 0
	v_pk_mul_f32 v[180:181], v[180:181], v[188:189]
	s_nop 0
	v_pk_fma_f32 v[180:181], v[180:181], v[182:183], v[180:181]
	v_med3_f32 v182, v28, s57, v234
	v_med3_f32 v183, v29, s57, v234
	v_pk_mul_f32 v[190:191], v[182:183], s[96:97] op_sel_hi:[1,0]
	v_cvt_pk_bf16_f32 v166, v180, v181
	v_add_co_u32_e32 v180, vcc, s2, v162
	v_exp_f32_e32 v190, v190
	v_exp_f32_e32 v191, v191
	v_med3_f32 v188, v112, s33, v234
	v_med3_f32 v189, v113, s33, v234
	v_addc_co_u32_e32 v181, vcc, 0, v163, vcc
	v_pk_add_f32 v[190:191], v[190:191], 1.0 op_sel_hi:[1,0]
	v_add_co_u32_e32 v162, vcc, 0x58000, v162
	v_rcp_f32_e32 v190, v190
	v_rcp_f32_e32 v191, v191
	v_addc_co_u32_e32 v163, vcc, 0, v163, vcc
	s_and_b64 vcc, exec, s[6:7]
	v_pk_mul_f32 v[182:183], v[182:183], v[190:191]
	s_nop 0
	v_pk_fma_f32 v[182:183], v[182:183], v[188:189], v[182:183]
	s_nop 0
	v_cvt_pk_bf16_f32 v167, v182, v183
	global_store_dwordx4 v[180:181], v[164:167], off
	s_nop 1
	v_med3_f32 v164, v6, s57, v234
	v_med3_f32 v165, v7, s57, v234
	v_pk_mul_f32 v[180:181], v[164:165], s[96:97] op_sel_hi:[1,0]
	v_med3_f32 v166, v118, s33, v234
	v_exp_f32_e32 v180, v180
	v_exp_f32_e32 v181, v181
	v_med3_f32 v167, v119, s33, v234
	v_pk_add_f32 v[180:181], v[180:181], 1.0 op_sel_hi:[1,0]
	s_nop 0
	v_rcp_f32_e32 v180, v180
	v_rcp_f32_e32 v181, v181
	s_nop 0
	v_pk_mul_f32 v[164:165], v[164:165], v[180:181]
	s_nop 0
	v_pk_fma_f32 v[164:165], v[164:165], v[166:167], v[164:165]
	v_med3_f32 v166, v8, s57, v234
	v_med3_f32 v167, v9, s57, v234
	v_pk_mul_f32 v[182:183], v[166:167], s[96:97] op_sel_hi:[1,0]
	v_med3_f32 v180, v120, s33, v234
	v_exp_f32_e32 v182, v182
	v_exp_f32_e32 v183, v183
	v_med3_f32 v181, v121, s33, v234
	v_cvt_pk_bf16_f32 v164, v164, v165
	v_pk_add_f32 v[182:183], v[182:183], 1.0 op_sel_hi:[1,0]
	s_nop 0
	v_rcp_f32_e32 v182, v182
	v_rcp_f32_e32 v183, v183
	s_nop 0
	v_pk_mul_f32 v[166:167], v[166:167], v[182:183]
	s_nop 0
	v_pk_fma_f32 v[166:167], v[166:167], v[180:181], v[166:167]
	v_med3_f32 v180, v2, s57, v234
	v_med3_f32 v181, v3, s57, v234
	v_pk_mul_f32 v[188:189], v[180:181], s[96:97] op_sel_hi:[1,0]
	v_med3_f32 v182, v126, s33, v234
	v_exp_f32_e32 v188, v188
	v_exp_f32_e32 v189, v189
	v_med3_f32 v183, v127, s33, v234
	v_cvt_pk_bf16_f32 v165, v166, v167
	v_pk_add_f32 v[188:189], v[188:189], 1.0 op_sel_hi:[1,0]
	s_nop 0
	v_rcp_f32_e32 v188, v188
	v_rcp_f32_e32 v189, v189
	s_nop 0
	v_pk_mul_f32 v[180:181], v[180:181], v[188:189]
	s_nop 0
	v_pk_fma_f32 v[180:181], v[180:181], v[182:183], v[180:181]
	v_med3_f32 v182, v4, s57, v234
	v_med3_f32 v183, v5, s57, v234
	v_pk_mul_f32 v[190:191], v[182:183], s[96:97] op_sel_hi:[1,0]
	v_med3_f32 v188, v128, s33, v234
	v_exp_f32_e32 v190, v190
	v_exp_f32_e32 v191, v191
	v_med3_f32 v189, v129, s33, v234
	v_cvt_pk_bf16_f32 v166, v180, v181
	v_pk_add_f32 v[190:191], v[190:191], 1.0 op_sel_hi:[1,0]
	s_nop 0
	v_rcp_f32_e32 v190, v190
	v_rcp_f32_e32 v191, v191
	s_nop 0
	v_pk_mul_f32 v[182:183], v[182:183], v[190:191]
	s_nop 0
	v_pk_fma_f32 v[182:183], v[182:183], v[188:189], v[182:183]
	s_nop 0
	v_cvt_pk_bf16_f32 v167, v182, v183
	global_store_dwordx4 v[162:163], v[164:167], off
	s_cbranch_vccnz .LBB0_1102
	s_andn2_b64 vcc, exec, s[26:27]
	s_cbranch_vccnz .LBB0_1080
	s_barrier
	s_branch .LBB0_1080

; __device__ __forceinline__ u32x4 pack8(const f32x4 v0, const f32x4 v1) { u32x4 w; w.x = cvt_pk_bf16(v0[0], v0[1]); w.y = cvt_pk_bf16(v0[2], v0[3]); w.z = cvt_pk_bf16(v1[0], v1[1]); w.w = cvt_pk_bf16(v1[2], v1[3]); return w; }
;     __device__ __forceinline__ void init(f32x4 (&acc)[2][2][4][2], const Pre& p) const {
; #pragma unroll
;         for (int bj = 0; bj < 2; ++bj)
; #pragma unroll
;             for (int a = 0; a < 2; ++a)
; #pragma unroll
;                 for (int m = 0; m < 4; ++m) { acc[a][bj][m][0] = p.v[2 * bj]; acc[a][bj][m][1] = p.v[2 * bj + 1]; } }
;     __device__ __forceinline__ void operator()(const f32x4 (&acc)[2][2][4][2], const Unit& u, int wr, int wc, int fr, int fq) const {
;         int rl0 = wr * 64 + fr; asm volatile("" : "+v"(rl0));
;         const int col0 = u.pn * BM + wc * 32 + 8 * fq;
;         int2 sr[2][4];
; #pragma unroll
;         for (int ai = 0; ai < 2; ++ai)
; #pragma unroll
;             for (int m = 0; m < 4; ++m) { const int rl = rl0 + ai * HALF + m * 16;
;                 sr[ai][m] = SLOT[(size_t)u.aux * GCAP_SLOTS + (size_t)u.lt * BM + (rl < u.rows ? rl : 0)]; }
;         __builtin_amdgcn_sched_barrier(0);
; #pragma unroll
;         for (int ai = 0; ai < 2; ++ai)
; #pragma unroll
;             for (int m = 0; m < 4; ++m) { const int rl = rl0 + ai * HALF + m * 16; const bool ok = rl < u.rows;
;                 const int2 s = sr[ai][m]; const float w = __int_as_float(s.y); bf16_t* rowp = YE + (size_t)(ok ? s.x : dummy_row) * 1024 + col0;
; #pragma unroll
;                 for (int bj = 0; bj < 2; ++bj) *(u32x4*)(rowp + bj * HALF) = pack8(acc[ai][bj][m][0] * w, acc[ai][bj][m][1] * w); }
.LBB0_1177:
	s_ashr_i32 s9, s8, 31
	s_lshl_b64 s[8:9], s[8:9], 12
	s_add_u32 s2, s43, s8
	s_addc_u32 s7, s44, s9
	s_lshl_b32 s8, s5, 8
	s_ashr_i32 s9, s8, 31
	s_lshl_b64 s[8:9], s[8:9], 2
	s_add_u32 s2, s2, s8
	s_addc_u32 s5, s7, s9
	s_add_u32 s8, s2, s46
	s_addc_u32 s9, s5, 0
	global_load_dwordx4 v[70:73], v166, s[8:9] offset:16
	global_load_dwordx4 v[78:81], v166, s[8:9]
	global_load_dwordx4 v[66:69], v166, s[8:9] offset:528
	global_load_dwordx4 v[74:77], v166, s[8:9] offset:512
	s_ashr_i32 s5, s4, 31
	v_mov_b32_e32 v164, v167
	s_ashr_i32 s7, s6, 31
	s_lshl_b64 s[4:5], s[4:5], 18
	s_add_u32 s2, s53, s4
	v_add_u32_e32 v160, 32, v164
	s_addc_u32 s8, s56, s5
	s_lshl_b64 s[4:5], s[6:7], 11
	v_cmp_gt_i32_e64 s[18:19], s65, v164
	v_add_u32_e32 v158, 16, v164
	v_cmp_gt_i32_e64 s[12:13], s65, v160
	v_add_u32_e32 v162, 48, v164
	s_add_u32 s68, s2, s4
	v_cndmask_b32_e64 v156, 0, v164, s[18:19]
	v_cmp_gt_i32_e64 s[14:15], s65, v158
	v_cndmask_b32_e64 v160, 0, v160, s[12:13]
	v_cmp_gt_i32_e64 s[10:11], s65, v162
	s_addc_u32 s69, s8, s5
	v_ashrrev_i32_e32 v157, 31, v156
	v_cndmask_b32_e64 v158, 0, v158, s[14:15]
	v_ashrrev_i32_e32 v161, 31, v160
	v_cndmask_b32_e64 v162, 0, v162, s[10:11]
	v_lshl_add_u64 v[156:157], v[156:157], 3, s[68:69]
	v_ashrrev_i32_e32 v159, 31, v158
	v_lshl_add_u64 v[160:161], v[160:161], 3, s[68:69]
	v_ashrrev_i32_e32 v163, 31, v162
	v_lshl_add_u64 v[158:159], v[158:159], 3, s[68:69]
	v_lshl_add_u64 v[162:163], v[162:163], 3, s[68:69]
	s_waitcnt vmcnt(12)
	v_mov_b64_e32 v[172:173], v[220:221]
	v_mov_b64_e32 v[174:175], v[222:223]
	v_mov_b64_e32 v[176:177], v[224:225]
	v_mov_b64_e32 v[178:179], v[226:227]
	v_add_u32_e32 v156, 0x80, v164
	v_add_u32_e32 v160, 0xa0, v164
	v_cmp_gt_i32_e64 s[8:9], s65, v156
	v_add_u32_e32 v158, 0x90, v164
	v_cmp_gt_i32_e64 s[4:5], s65, v160
	v_add_u32_e32 v162, 0xb0, v164
	v_cndmask_b32_e64 v156, 0, v156, s[8:9]
	v_cmp_gt_i32_e64 s[6:7], s65, v158
	v_cndmask_b32_e64 v160, 0, v160, s[4:5]
	v_cmp_gt_i32_e32 vcc, s65, v162
	v_ashrrev_i32_e32 v157, 31, v156
	v_cndmask_b32_e64 v158, 0, v158, s[6:7]
	v_ashrrev_i32_e32 v161, 31, v160
	v_cndmask_b32_e32 v162, 0, v162, vcc
	v_lshl_add_u64 v[156:157], v[156:157], 3, s[68:69]
	v_ashrrev_i32_e32 v159, 31, v158
	v_lshl_add_u64 v[160:161], v[160:161], 3, s[68:69]
	v_ashrrev_i32_e32 v163, 31, v162
	v_lshl_add_u64 v[158:159], v[158:159], 3, s[68:69]
	v_lshl_add_u64 v[180:181], v[162:163], 3, s[68:69]
	v_mov_b64_e32 v[164:165], v[240:241]
	v_mov_b64_e32 v[162:163], v[242:243]
	s_nop 0
	v_mov_b64_e32 v[160:161], v[244:245]
	s_nop 0
	v_mov_b64_e32 v[156:157], v[246:247]
	v_lshl_or_b32 v158, s66, 8, v169
	v_cndmask_b32_e64 v180, v250, v172, s[18:19]
	v_ashrrev_i32_e32 v181, 31, v180
	v_ashrrev_i32_e32 v159, 31, v158
	v_lshlrev_b64 v[180:181], 11, v[180:181]
	v_lshl_add_u64 v[180:181], s[22:23], 0, v[180:181]
	v_lshlrev_b64 v[158:159], 1, v[158:159]
	v_lshl_add_u64 v[180:181], v[180:181], 0, v[158:159]
	v_pk_mul_f32 v[144:145], v[144:145], v[172:173] op_sel:[0,1]
	v_pk_mul_f32 v[142:143], v[142:143], v[172:173] op_sel:[0,1]
	v_pk_mul_f32 v[182:183], v[140:141], v[172:173] op_sel:[0,1]
	v_pk_mul_f32 v[140:141], v[138:139], v[172:173] op_sel:[0,1]
	v_cvt_pk_bf16_f32 v138, v142, v143
	v_cvt_pk_bf16_f32 v139, v144, v145
	v_pk_mul_f32 v[134:135], v[134:135], v[172:173] op_sel:[0,1]
	v_cvt_pk_bf16_f32 v140, v140, v141
	v_cvt_pk_bf16_f32 v141, v182, v183
	global_store_dwordx4 v[180:181], v[138:141], off
	v_pk_mul_f32 v[136:137], v[136:137], v[172:173] op_sel:[0,1]
	v_pk_mul_f32 v[128:129], v[128:129], v[174:175] op_sel:[0,1]
	v_pk_mul_f32 v[138:139], v[132:133], v[172:173] op_sel:[0,1]
	v_pk_mul_f32 v[132:133], v[130:131], v[172:173] op_sel:[0,1]
	v_cvt_pk_bf16_f32 v130, v134, v135
	v_cvt_pk_bf16_f32 v131, v136, v137
	v_pk_mul_f32 v[126:127], v[126:127], v[174:175] op_sel:[0,1]
	v_cvt_pk_bf16_f32 v132, v132, v133
	v_cvt_pk_bf16_f32 v133, v138, v139
	global_store_dwordx4 v[180:181], v[130:133], off offset:256
	v_pk_mul_f32 v[118:119], v[118:119], v[174:175] op_sel:[0,1]
	v_pk_mul_f32 v[120:121], v[120:121], v[174:175] op_sel:[0,1]
	v_cndmask_b32_e64 v130, v250, v174, s[14:15]
	v_ashrrev_i32_e32 v131, 31, v130
	v_lshlrev_b64 v[130:131], 11, v[130:131]
	v_lshl_add_u64 v[130:131], s[22:23], 0, v[130:131]
	v_lshl_add_u64 v[130:131], v[130:131], 0, v[158:159]
	v_pk_mul_f32 v[132:133], v[124:125], v[174:175] op_sel:[0,1]
	v_pk_mul_f32 v[124:125], v[122:123], v[174:175] op_sel:[0,1]
	v_cvt_pk_bf16_f32 v122, v126, v127
	v_cvt_pk_bf16_f32 v123, v128, v129
	v_pk_mul_f32 v[112:113], v[112:113], v[176:177] op_sel:[0,1]
	v_cvt_pk_bf16_f32 v124, v124, v125
	v_cvt_pk_bf16_f32 v125, v132, v133
	global_store_dwordx4 v[130:131], v[122:125], off
	v_pk_mul_f32 v[110:111], v[110:111], v[176:177] op_sel:[0,1]
	v_pk_mul_f32 v[102:103], v[102:103], v[176:177] op_sel:[0,1]
	v_pk_mul_f32 v[122:123], v[116:117], v[174:175] op_sel:[0,1]
	v_pk_mul_f32 v[116:117], v[114:115], v[174:175] op_sel:[0,1]
	v_cvt_pk_bf16_f32 v114, v118, v119
	v_cvt_pk_bf16_f32 v115, v120, v121
	v_pk_mul_f32 v[104:105], v[104:105], v[176:177] op_sel:[0,1]
	v_cvt_pk_bf16_f32 v116, v116, v117
	v_cvt_pk_bf16_f32 v117, v122, v123
	global_store_dwordx4 v[130:131], v[114:117], off offset:256
	v_pk_mul_f32 v[96:97], v[96:97], v[178:179] op_sel:[0,1]
	v_pk_mul_f32 v[94:95], v[94:95], v[178:179] op_sel:[0,1]
	v_cndmask_b32_e64 v114, v250, v176, s[12:13]
	v_ashrrev_i32_e32 v115, 31, v114
	v_lshlrev_b64 v[114:115], 11, v[114:115]
	v_lshl_add_u64 v[114:115], s[22:23], 0, v[114:115]
	v_lshl_add_u64 v[114:115], v[114:115], 0, v[158:159]
	v_pk_mul_f32 v[116:117], v[108:109], v[176:177] op_sel:[0,1]
	v_pk_mul_f32 v[108:109], v[106:107], v[176:177] op_sel:[0,1]
; __device__ __forceinline__ u32x4 pack8(const f32x4 v0, const f32x4 v1) { u32x4 w; w.x = cvt_pk_bf16(v0[0], v0[1]); w.y = cvt_pk_bf16(v0[2], v0[3]); w.z = cvt_pk_bf16(v1[0], v1[1]); w.w = cvt_pk_bf16(v1[2], v1[3]); return w; }
; #define PG8_BAR __builtin_amdgcn_s_barrier()
;     __device__ __forceinline__ void operator()(const f32x4 (&acc)[2][2][4][2], const Unit& u, int wr, int wc, int fr, int fq) const {
;     ...
; #pragma unroll
;         for (int ai = 0; ai < 2; ++ai)
; #pragma unroll
;             for (int m = 0; m < 4; ++m) { const int rl = rl0 + ai * HALF + m * 16; const bool ok = rl < u.rows;
;                 const int2 s = sr[ai][m]; const float w = __int_as_float(s.y); bf16_t* rowp = YE + (size_t)(ok ? s.x : dummy_row) * 1024 + col0;
; #pragma unroll
;                 for (int bj = 0; bj < 2; ++bj) *(u32x4*)(rowp + bj * HALF) = pack8(acc[ai][bj][m][0] * w, acc[ai][bj][m][1] * w); }
; template <class Epi, class Sched, bool ALIGN_EPI = false, bool SP2 = false, bool GATHER = false>
; __device__ __forceinline__ void gemm_phase(PG8_LAS unsigned char* lds, const Gemm g, const Sched& S, const Epi& E, const int2* gslot = nullptr, PG8_LAS unsigned char* gtab = nullptr) {
;     ...
;         if constexpr (!Epi::AFTER_DRAIN) { E(acc, cur, wr, wc, fr, fq); S.done(cur); }
;         if (!has_next) break;
;         E.init(acc, pre);
;         cur = nxt; cA = nA; cB = nB; ++ui;
;         if constexpr (GATHER) { _Pragma("unroll") for (int h_ = 0; h_ < 2; ++h_) _Pragma("unroll") for (int i_ = 0; i_ < 2; ++i_) vC[h_][i_] = vN[h_][i_]; }
;         if constexpr (ALIGN_EPI) { if (wr == 1) PG8_BAR; }
	v_cvt_pk_bf16_f32 v106, v110, v111
	v_cvt_pk_bf16_f32 v107, v112, v113
	v_pk_mul_f32 v[86:87], v[86:87], v[178:179] op_sel:[0,1]
	v_cvt_pk_bf16_f32 v108, v108, v109
	v_cvt_pk_bf16_f32 v109, v116, v117
	global_store_dwordx4 v[114:115], v[106:109], off
	v_pk_mul_f32 v[88:89], v[88:89], v[178:179] op_sel:[0,1]
	v_pk_mul_f32 v[64:65], v[64:65], v[164:165] op_sel:[0,1]
	v_pk_mul_f32 v[106:107], v[100:101], v[176:177] op_sel:[0,1]
	v_pk_mul_f32 v[100:101], v[98:99], v[176:177] op_sel:[0,1]
	v_cvt_pk_bf16_f32 v98, v102, v103
	v_cvt_pk_bf16_f32 v99, v104, v105
	v_pk_mul_f32 v[62:63], v[62:63], v[164:165] op_sel:[0,1]
	v_cvt_pk_bf16_f32 v100, v100, v101
	v_cvt_pk_bf16_f32 v101, v106, v107
	global_store_dwordx4 v[114:115], v[98:101], off offset:256
	v_pk_mul_f32 v[54:55], v[54:55], v[164:165] op_sel:[0,1]
	v_pk_mul_f32 v[56:57], v[56:57], v[164:165] op_sel:[0,1]
	v_cndmask_b32_e64 v98, v250, v178, s[10:11]
	v_ashrrev_i32_e32 v99, 31, v98
	v_lshlrev_b64 v[98:99], 11, v[98:99]
	v_lshl_add_u64 v[98:99], s[22:23], 0, v[98:99]
	v_lshl_add_u64 v[98:99], v[98:99], 0, v[158:159]
	v_pk_mul_f32 v[100:101], v[92:93], v[178:179] op_sel:[0,1]
	v_pk_mul_f32 v[92:93], v[90:91], v[178:179] op_sel:[0,1]
	v_cvt_pk_bf16_f32 v90, v94, v95
	v_cvt_pk_bf16_f32 v91, v96, v97
	v_pk_mul_f32 v[48:49], v[48:49], v[162:163] op_sel:[0,1]
	v_cvt_pk_bf16_f32 v92, v92, v93
	v_cvt_pk_bf16_f32 v93, v100, v101
	global_store_dwordx4 v[98:99], v[90:93], off
	v_pk_mul_f32 v[46:47], v[46:47], v[162:163] op_sel:[0,1]
	v_pk_mul_f32 v[38:39], v[38:39], v[162:163] op_sel:[0,1]
	v_pk_mul_f32 v[90:91], v[84:85], v[178:179] op_sel:[0,1]
	v_pk_mul_f32 v[84:85], v[82:83], v[178:179] op_sel:[0,1]
	v_cvt_pk_bf16_f32 v82, v86, v87
	v_cvt_pk_bf16_f32 v83, v88, v89
	v_pk_mul_f32 v[40:41], v[40:41], v[162:163] op_sel:[0,1]
	v_cvt_pk_bf16_f32 v84, v84, v85
	v_cvt_pk_bf16_f32 v85, v90, v91
	global_store_dwordx4 v[98:99], v[82:85], off offset:256
	v_pk_mul_f32 v[32:33], v[32:33], v[160:161] op_sel:[0,1]
	v_pk_mul_f32 v[30:31], v[30:31], v[160:161] op_sel:[0,1]
	v_cndmask_b32_e64 v82, v250, v164, s[8:9]
	v_ashrrev_i32_e32 v83, 31, v82
	v_lshlrev_b64 v[82:83], 11, v[82:83]
	v_lshl_add_u64 v[82:83], s[22:23], 0, v[82:83]
	v_lshl_add_u64 v[82:83], v[82:83], 0, v[158:159]
	v_pk_mul_f32 v[84:85], v[60:61], v[164:165] op_sel:[0,1]
	v_pk_mul_f32 v[60:61], v[58:59], v[164:165] op_sel:[0,1]
	v_cvt_pk_bf16_f32 v58, v62, v63
	v_cvt_pk_bf16_f32 v59, v64, v65
	v_pk_mul_f32 v[22:23], v[22:23], v[160:161] op_sel:[0,1]
	v_cvt_pk_bf16_f32 v60, v60, v61
	v_cvt_pk_bf16_f32 v61, v84, v85
	s_waitcnt vmcnt(0)
	global_store_dwordx4 v[82:83], v[58:61], off
	v_pk_mul_f32 v[24:25], v[24:25], v[160:161] op_sel:[0,1]
	v_pk_mul_f32 v[16:17], v[16:17], v[156:157] op_sel:[0,1]
	v_pk_mul_f32 v[58:59], v[52:53], v[164:165] op_sel:[0,1]
	v_pk_mul_f32 v[52:53], v[50:51], v[164:165] op_sel:[0,1]
	v_cvt_pk_bf16_f32 v50, v54, v55
	v_cvt_pk_bf16_f32 v51, v56, v57
	v_pk_mul_f32 v[14:15], v[14:15], v[156:157] op_sel:[0,1]
	v_cvt_pk_bf16_f32 v52, v52, v53
	v_cvt_pk_bf16_f32 v53, v58, v59
	global_store_dwordx4 v[82:83], v[50:53], off offset:256
	v_pk_mul_f32 v[8:9], v[8:9], v[156:157] op_sel:[0,1]
	v_pk_mul_f32 v[6:7], v[6:7], v[156:157] op_sel:[0,1]
	v_cndmask_b32_e64 v50, v250, v162, s[6:7]
	v_ashrrev_i32_e32 v51, 31, v50
	v_lshlrev_b64 v[50:51], 11, v[50:51]
	v_lshl_add_u64 v[50:51], s[22:23], 0, v[50:51]
	v_lshl_add_u64 v[50:51], v[50:51], 0, v[158:159]
	v_pk_mul_f32 v[52:53], v[44:45], v[162:163] op_sel:[0,1]
	v_pk_mul_f32 v[44:45], v[42:43], v[162:163] op_sel:[0,1]
	v_cvt_pk_bf16_f32 v42, v46, v47
	v_cvt_pk_bf16_f32 v43, v48, v49
	s_nop 0
	v_cvt_pk_bf16_f32 v44, v44, v45
	v_cvt_pk_bf16_f32 v45, v52, v53
	global_store_dwordx4 v[50:51], v[42:45], off
	s_nop 1
	v_pk_mul_f32 v[42:43], v[36:37], v[162:163] op_sel:[0,1]
	v_pk_mul_f32 v[36:37], v[34:35], v[162:163] op_sel:[0,1]
	v_cvt_pk_bf16_f32 v34, v38, v39
	v_cvt_pk_bf16_f32 v35, v40, v41
	s_nop 0
	v_cvt_pk_bf16_f32 v36, v36, v37
	v_cvt_pk_bf16_f32 v37, v42, v43
	global_store_dwordx4 v[50:51], v[34:37], off offset:256
	s_nop 1
	v_cndmask_b32_e64 v34, v250, v160, s[4:5]
	v_ashrrev_i32_e32 v35, 31, v34
	v_lshlrev_b64 v[34:35], 11, v[34:35]
	v_lshl_add_u64 v[34:35], s[22:23], 0, v[34:35]
	v_lshl_add_u64 v[34:35], v[34:35], 0, v[158:159]
	v_pk_mul_f32 v[36:37], v[28:29], v[160:161] op_sel:[0,1]
	v_pk_mul_f32 v[28:29], v[26:27], v[160:161] op_sel:[0,1]
	v_cvt_pk_bf16_f32 v26, v30, v31
	v_cvt_pk_bf16_f32 v27, v32, v33
	s_mov_b64 s[4:5], -1
	v_cvt_pk_bf16_f32 v28, v28, v29
	v_cvt_pk_bf16_f32 v29, v36, v37
	global_store_dwordx4 v[34:35], v[26:29], off
	s_nop 1
	v_pk_mul_f32 v[26:27], v[20:21], v[160:161] op_sel:[0,1]
	v_pk_mul_f32 v[20:21], v[18:19], v[160:161] op_sel:[0,1]
	v_cvt_pk_bf16_f32 v18, v22, v23
	v_cvt_pk_bf16_f32 v19, v24, v25
	s_nop 0
	v_cvt_pk_bf16_f32 v20, v20, v21
	v_cvt_pk_bf16_f32 v21, v26, v27
	global_store_dwordx4 v[34:35], v[18:21], off offset:256
	s_nop 1
	v_cndmask_b32_e32 v18, v250, v156, vcc
	v_ashrrev_i32_e32 v19, 31, v18
	v_lshlrev_b64 v[18:19], 11, v[18:19]
	v_lshl_add_u64 v[18:19], s[22:23], 0, v[18:19]
	v_lshl_add_u64 v[18:19], v[18:19], 0, v[158:159]
	v_pk_mul_f32 v[20:21], v[12:13], v[156:157] op_sel:[0,1]
	v_pk_mul_f32 v[12:13], v[10:11], v[156:157] op_sel:[0,1]
	v_cvt_pk_bf16_f32 v10, v14, v15
	v_cvt_pk_bf16_f32 v11, v16, v17
	s_andn2_b64 vcc, exec, s[30:31]
	v_cvt_pk_bf16_f32 v12, v12, v13
	v_cvt_pk_bf16_f32 v13, v20, v21
	global_store_dwordx4 v[18:19], v[10:13], off
	s_nop 1
	v_pk_mul_f32 v[10:11], v[4:5], v[156:157] op_sel:[0,1]
	v_pk_mul_f32 v[4:5], v[2:3], v[156:157] op_sel:[0,1]
	v_cvt_pk_bf16_f32 v2, v6, v7
	v_cvt_pk_bf16_f32 v3, v8, v9
	s_nop 0
	v_cvt_pk_bf16_f32 v4, v4, v5
	v_cvt_pk_bf16_f32 v5, v10, v11
	global_store_dwordx4 v[18:19], v[2:5], off offset:256
	s_cbranch_vccnz .LBB0_1166
	s_andn2_b64 vcc, exec, s[20:21]
	s_cbranch_vccnz .LBB0_1165
	s_barrier
	s_branch .LBB0_1165
